# deferred weight-conversion split: 2600 + 1300 tiles deferred, idle-slot quotas 6/6/7/8
# baseline (speedup 1.0000x reference)
; #define SEAM(k) do { if (IN(k) && IN((k) + 1)) xcd_barrier(bar); \
;         if (PROBE_MASK) { const unsigned long long t_ = __builtin_amdgcn_s_memrealtime(); if ((PROBE_MASK >> (k)) & 1u) pr_acc += t_ - pr_t0; pr_t0 = t_; } } while (0)
; __device__ __forceinline__ void convert_deferred(const Ptrs& P, unsigned char* lds, int quota) {
;     const int tid = threadIdx.x, wid = tid >> 6, lane = tid & 63;
;     float* tile = (float*)lds;
;     volatile __attribute__((address_space(3))) int* slot = (volatile __attribute__((address_space(3))) int*)((__attribute__((address_space(3))) unsigned char*)lds + 131072 + 320 + 11000);
;     unsigned* q = (unsigned*)(P.ws + WS_CTL) + CW_DEFQ;
;     for (int n = 0; n < quota; ++n) {
;         __syncthreads();
;         if (tid == 0) *slot = (int)atomicAdd(q, 1u);
;         __syncthreads();
;         const int t = *slot;
;         if (t >= DEF_GU + DEF_DN) break;
;         const bool gu = t < DEF_GU;
;         const float* src = gu ? P.in[34] : P.in[36]; bf16* dst = (bf16*)(P.ws + (gu ? WS_WGU : WS_WDN));
;         const int N = gu ? 2048 : 1024, ntn = N / 256, it = gu ? 2 * NE * 16 * 8 - DEF_GU + t : 2 * NE * 16 * 4 - DEF_DN + (t - DEF_GU);
; __global__ void __launch_bounds__(NT, 2) mega(Args args) {
;     ...
;     if (IN(6)) { g8::DenseOrder S; S.init(MIX, D, (const bf16*)(ws + WS_WEVOUT), D, R, D, G, (int)blockIdx.x, 0); g8::EpiOut E{P, 0};
;         g8::gemm_phase<g8::EpiOut, g8::DenseOrder, false, true>(LDSP, D, D, S, E);
;         if (IDLE_LAST(68 * 4)) convert_deferred(P, lds, 4); } SEAM(6);
.LBB0_1286:
	s_abs_i32 s3, s62
	v_cvt_f32_u32_e32 v2, s3
	s_sub_i32 s4, 0, s3
	s_mov_b32 s5, 0
	v_rcp_iflag_f32_e32 v2, v2
	s_nop 0
	v_mul_f32_e32 v2, 0x4f7ffffe, v2
	v_cvt_u32_f32_e32 v2, v2
	s_nop 0
	v_readfirstlane_b32 s6, v2
	s_mul_i32 s4, s4, s6
	s_mul_hi_u32 s4, s6, s4
	s_add_i32 s6, s6, s4
	s_mul_hi_u32 s4, s6, 0x110
	s_mul_i32 s4, s4, s3
	s_sub_i32 s4, 0x110, s4
	s_sub_i32 s6, s4, s3
	s_cmp_ge_u32 s4, s3
	s_cselect_b32 s4, s6, s4
	s_sub_i32 s6, s4, s3
	s_cmp_ge_u32 s4, s3
	s_cselect_b32 s3, s6, s4
	s_cmp_eq_u32 s3, 0
	s_cselect_b64 s[6:7], -1, 0
	s_cmp_lt_i32 s2, s3
	s_cselect_b64 s[8:9], -1, 0
	s_or_b64 s[6:7], s[6:7], s[8:9]
	s_and_b64 vcc, exec, s[6:7]
	s_cbranch_vccnz .LBB0_1296
	v_and_b32_e32 v2, 0x7c, v188
	v_lshlrev_b32_e32 v3, 5, v0
	s_movk_i32 s3, 0x400
	v_and_or_b32 v12, v3, s3, v2
	v_bfe_u32 v2, v0, 3, 3
	v_lshl_or_b32 v4, v1, 5, v2
	v_lshlrev_b32_e32 v2, 3, v0
	v_lshl_add_u32 v11, v182, 4, 0
	v_and_b32_e32 v2, 56, v2
	v_mul_u32_u24_e32 v16, 0x2020, v1
	v_mov_b32_e32 v3, 0
	v_lshl_add_u32 v27, v4, 2, 0
	v_mul_u32_u24_e32 v28, 0x404, v2
	v_lshlrev_b32_e32 v10, 6, v4
	s_add_i32 s12, 0, 0x22c38
	v_add_u32_e32 v16, v11, v16
	v_and_b32_e32 v13, 0xfc, v188
	v_and_b32_e32 v14, 56, v185
	s_mov_b32 s3, 6
	v_or_b32_e32 v4, 0x200, v10
	v_mov_b32_e32 v5, v3
	v_or_b32_e32 v6, 0x400, v10
	v_mov_b32_e32 v7, v3
	v_or_b32_e32 v8, 0x600, v10
	v_mov_b32_e32 v9, v3
	v_mov_b32_e32 v15, s12
	s_movk_i32 s13, 0xf3b
	s_movk_i32 s14, 0x800
	s_mov_b32 s15, 0x1104e000
	s_movk_i32 s16, 0xc4
	v_add_u32_e32 v17, 0x404, v16
	v_add_u32_e32 v18, 0x40c, v16
	v_add_u32_e32 v19, 0x808, v16
	v_add_u32_e32 v20, 0xc0c, v16
	v_add_u32_e32 v21, 0xc14, v16
	v_add_u32_e32 v22, 0x1414, v16
	v_add_u32_e32 v23, 0x141c, v16
	v_add_u32_e32 v24, 0x1818, v16
	v_add_u32_e32 v25, 0x1c1c, v16
	v_add_u32_e32 v26, 0x1c24, v16
	v_lshlrev_b32_e32 v2, 1, v2
	v_add_u32_e32 v27, v27, v28
	v_lshlrev_b32_e32 v10, 1, v10
	s_branch .LBB0_1289
